# speedup vs baseline: 1.0125x; 1.0125x over previous
.Lit_Af:
	ds_read_b64 v[68:69], v88
	ds_read_b64 v[70:71], v89
	ds_read_b64 v[72:73], v90
	ds_read_b64 v[74:75], v91
	v_add_u32_sdwa v92, v105, v52 dst_sel:DWORD dst_unused:UNUSED_PAD src0_sel:DWORD src1_sel:WORD_0
	v_add_u32_sdwa v93, v105, v52 dst_sel:DWORD dst_unused:UNUSED_PAD src0_sel:DWORD src1_sel:WORD_1
	v_add_u32_sdwa v106, v105, v53 dst_sel:DWORD dst_unused:UNUSED_PAD src0_sel:DWORD src1_sel:WORD_0
	v_add_u32_sdwa v107, v105, v53 dst_sel:DWORD dst_unused:UNUSED_PAD src0_sel:DWORD src1_sel:WORD_1
	v_add_u32_sdwa v108, v105, v54 dst_sel:DWORD dst_unused:UNUSED_PAD src0_sel:DWORD src1_sel:WORD_0
	v_add_u32_sdwa v109, v105, v54 dst_sel:DWORD dst_unused:UNUSED_PAD src0_sel:DWORD src1_sel:WORD_1
	v_add_u32_sdwa v88, v105, v55 dst_sel:DWORD dst_unused:UNUSED_PAD src0_sel:DWORD src1_sel:WORD_0
	v_add_u32_sdwa v89, v105, v55 dst_sel:DWORD dst_unused:UNUSED_PAD src0_sel:DWORD src1_sel:WORD_1
	ds_read_b128 v[120:123], v92
	ds_read_b128 v[124:127], v93
	ds_read_b128 v[128:131], v106
	ds_read_b128 v[132:135], v107
	ds_read_b128 v[140:143], v108
	ds_read_b128 v[144:147], v109
	ds_read_b128 v[148:151], v88
	ds_read_b128 v[152:155], v89
	s_waitcnt lgkmcnt(11)
	v_pk_add_f32 v[76:77], v[44:45], v[68:69]
	s_waitcnt lgkmcnt(9)
	v_pk_add_f32 v[78:79], v[70:71], v[72:73]
	s_waitcnt lgkmcnt(8)
	v_pk_add_f32 v[76:77], v[76:77], v[74:75]
	ds_read_b128 v[46:49], v138 offset:56896
	v_pk_add_f32 v[76:77], v[76:77], v[78:79]
	ds_read_b64 v[50:51], v139
	v_pk_mul_f32 v[78:79], v[40:41], v[76:77] op_sel_hi:[0,1]
	v_cmp_eq_u32_e64 s[6:7], 1, v117
	ds_write_b64 v137, v[78:79]
	ds_read2_b64 v[56:59], v156 offset1:2
	ds_read_b64 v[82:83], v118
	ds_read_b64 v[84:85], v119
	ds_read_b64 v[86:87], v136
	s_waitcnt lgkmcnt(6)
	v_pk_add_f32 v[120:121], v[120:121], v[124:125]
	v_pk_add_f32 v[122:123], v[122:123], v[126:127]
	v_pk_add_f32 v[128:129], v[128:129], v[132:133]
	v_pk_add_f32 v[130:131], v[130:131], v[134:135]
	v_pk_add_f32 v[140:141], v[140:141], v[144:145]
	v_pk_add_f32 v[142:143], v[142:143], v[146:147]
	v_pk_add_f32 v[148:149], v[148:149], v[152:153]
	v_pk_add_f32 v[150:151], v[150:151], v[154:155]
	v_pk_add_f32 v[120:121], v[120:121], v[128:129]
	v_pk_add_f32 v[122:123], v[122:123], v[130:131]
	v_pk_add_f32 v[140:141], v[140:141], v[148:149]
	v_pk_add_f32 v[142:143], v[142:143], v[150:151]
	v_pk_add_f32 v[120:121], v[120:121], v[140:141]
	v_pk_add_f32 v[122:123], v[122:123], v[142:143]
	v_add_u32_e32 v138, 0xfffffe00, v138
	v_add_u32_e32 v139, 0xffffff00, v139
	v_permlane32_swap_b32_e32 v120, v122
	v_permlane32_swap_b32_e32 v121, v123
	v_pk_add_f32 v[62:63], v[120:121], v[122:123]
	s_mov_b64 exec, s[6:7]
	s_waitcnt lgkmcnt(2)
	v_pk_fma_f32 v[80:81], v[40:41], v[82:83], v[78:79] op_sel_hi:[0,1,1]
	s_waitcnt lgkmcnt(1)
	v_pk_fma_f32 v[80:81], v[40:41], v[84:85], v[80:81] op_sel_hi:[0,1,1]
	s_waitcnt lgkmcnt(0)
	v_pk_fma_f32 v[80:81], v[40:41], v[86:87], v[80:81] op_sel_hi:[0,1,1]
	ds_write_b64 v137, v[80:81]
	s_mov_b64 exec, -1
	s_cmp_lt_u32 s9, 2
	s_cbranch_scc1 .Lnp_Af
	v_cmp_eq_u32_e64 s[6:7], 2, v117
	s_nop 0
	s_mov_b64 exec, s[6:7]
	ds_read_b64 v[82:83], v118
	ds_read_b64 v[84:85], v119
	ds_read_b64 v[86:87], v136
	s_mov_b64 exec, -1
	v_add_u32_sdwa v88, v116, v50 dst_sel:DWORD dst_unused:UNUSED_PAD src0_sel:DWORD src1_sel:WORD_0
	v_add_u32_sdwa v89, v116, v50 dst_sel:DWORD dst_unused:UNUSED_PAD src0_sel:DWORD src1_sel:WORD_1
	v_add_u32_sdwa v90, v116, v51 dst_sel:DWORD dst_unused:UNUSED_PAD src0_sel:DWORD src1_sel:WORD_0
	v_add_u32_sdwa v91, v116, v51 dst_sel:DWORD dst_unused:UNUSED_PAD src0_sel:DWORD src1_sel:WORD_1
	v_bfe_u32 v168, v49, 16, 7
	v_add_u32_sdwa v169, v116, v47 dst_sel:DWORD dst_unused:UNUSED_PAD src0_sel:DWORD src1_sel:WORD_0
	v_add_u32_sdwa v170, v116, v47 dst_sel:DWORD dst_unused:UNUSED_PAD src0_sel:DWORD src1_sel:WORD_1
	v_add_u32_sdwa v171, v116, v49 dst_sel:DWORD dst_unused:UNUSED_PAD src0_sel:DWORD src1_sel:WORD_0
	v_add_u32_e32 v156, 0xfffffa00, v156
	v_add_u32_e32 v172, 0xfffffe00, v137
	v_readlane_b32 s4, v60, s5
	v_max_i32_e32 v156, v156, v162
	v_lshl_add_u64 v[158:159], v[158:159], 0, s[2:3]
	s_or_b32 s10, s21, s4
	s_and_b32 s10, s10, 0x700
	s_and_b32 s23, s21, 0xff
	s_cselect_b32 s24, 0, 0x700
	s_or_b32 s10, s10, s24
	s_mov_b64 exec, s[6:7]
	s_waitcnt lgkmcnt(2)
	v_pk_fma_f32 v[80:81], v[40:41], v[82:83], v[78:79] op_sel_hi:[0,1,1]
	s_waitcnt lgkmcnt(1)
	v_pk_fma_f32 v[80:81], v[40:41], v[84:85], v[80:81] op_sel_hi:[0,1,1]
	s_waitcnt lgkmcnt(0)
	v_pk_fma_f32 v[80:81], v[40:41], v[86:87], v[80:81] op_sel_hi:[0,1,1]
	ds_write_b64 v137, v[80:81]
	s_mov_b64 exec, -1
	s_cmp_lt_u32 s9, 3
	s_cbranch_scc1 .Lbot_A
	s_mov_b32 s8, 3

.Lit_Bf:
	ds_read_b64 v[68:69], v88
	ds_read_b64 v[70:71], v89
	ds_read_b64 v[72:73], v90
	ds_read_b64 v[74:75], v91
	v_add_u32_sdwa v92, v105, v56 dst_sel:DWORD dst_unused:UNUSED_PAD src0_sel:DWORD src1_sel:WORD_0
	v_add_u32_sdwa v93, v105, v56 dst_sel:DWORD dst_unused:UNUSED_PAD src0_sel:DWORD src1_sel:WORD_1
	v_add_u32_sdwa v106, v105, v57 dst_sel:DWORD dst_unused:UNUSED_PAD src0_sel:DWORD src1_sel:WORD_0
	v_add_u32_sdwa v107, v105, v57 dst_sel:DWORD dst_unused:UNUSED_PAD src0_sel:DWORD src1_sel:WORD_1
	v_add_u32_sdwa v108, v105, v58 dst_sel:DWORD dst_unused:UNUSED_PAD src0_sel:DWORD src1_sel:WORD_0
	v_add_u32_sdwa v109, v105, v58 dst_sel:DWORD dst_unused:UNUSED_PAD src0_sel:DWORD src1_sel:WORD_1
	v_add_u32_sdwa v88, v105, v59 dst_sel:DWORD dst_unused:UNUSED_PAD src0_sel:DWORD src1_sel:WORD_0
	v_add_u32_sdwa v89, v105, v59 dst_sel:DWORD dst_unused:UNUSED_PAD src0_sel:DWORD src1_sel:WORD_1
	ds_read_b128 v[120:123], v92
	ds_read_b128 v[124:127], v93
	ds_read_b128 v[128:131], v106
	ds_read_b128 v[132:135], v107
	ds_read_b128 v[140:143], v108
	ds_read_b128 v[144:147], v109
	ds_read_b128 v[148:151], v88
	ds_read_b128 v[152:155], v89
	s_waitcnt lgkmcnt(11)
	v_pk_add_f32 v[76:77], v[62:63], v[68:69]
	s_waitcnt lgkmcnt(9)
	v_pk_add_f32 v[78:79], v[70:71], v[72:73]
	s_waitcnt lgkmcnt(8)
	v_pk_add_f32 v[76:77], v[76:77], v[74:75]
	ds_read_b128 v[38:41], v138 offset:56896
	v_pk_add_f32 v[76:77], v[76:77], v[78:79]
	ds_read_b64 v[42:43], v139
	v_pk_mul_f32 v[78:79], v[48:49], v[76:77] op_sel_hi:[0,1]
	v_cmp_eq_u32_e64 s[6:7], 1, v168
	ds_write_b64 v172, v[78:79]
	ds_read2_b64 v[52:55], v156 offset1:2
	ds_read_b64 v[82:83], v169
	ds_read_b64 v[84:85], v170
	ds_read_b64 v[86:87], v171
	s_waitcnt lgkmcnt(6)
	v_pk_add_f32 v[120:121], v[120:121], v[124:125]
	v_pk_add_f32 v[122:123], v[122:123], v[126:127]
	v_pk_add_f32 v[128:129], v[128:129], v[132:133]
	v_pk_add_f32 v[130:131], v[130:131], v[134:135]
	v_pk_add_f32 v[140:141], v[140:141], v[144:145]
	v_pk_add_f32 v[142:143], v[142:143], v[146:147]
	v_pk_add_f32 v[148:149], v[148:149], v[152:153]
	v_pk_add_f32 v[150:151], v[150:151], v[154:155]
	v_pk_add_f32 v[120:121], v[120:121], v[128:129]
	v_pk_add_f32 v[122:123], v[122:123], v[130:131]
	v_pk_add_f32 v[140:141], v[140:141], v[148:149]
	v_pk_add_f32 v[142:143], v[142:143], v[150:151]
	v_pk_add_f32 v[120:121], v[120:121], v[140:141]
	v_pk_add_f32 v[122:123], v[122:123], v[142:143]
	v_add_u32_e32 v138, 0xfffffe00, v138
	v_add_u32_e32 v139, 0xffffff00, v139
	v_permlane32_swap_b32_e32 v120, v122
	v_permlane32_swap_b32_e32 v121, v123
	v_pk_add_f32 v[44:45], v[120:121], v[122:123]
	s_mov_b64 exec, s[6:7]
	s_waitcnt lgkmcnt(2)
	v_pk_fma_f32 v[80:81], v[48:49], v[82:83], v[78:79] op_sel_hi:[0,1,1]
	s_waitcnt lgkmcnt(1)
	v_pk_fma_f32 v[80:81], v[48:49], v[84:85], v[80:81] op_sel_hi:[0,1,1]
	s_waitcnt lgkmcnt(0)
	v_pk_fma_f32 v[80:81], v[48:49], v[86:87], v[80:81] op_sel_hi:[0,1,1]
	ds_write_b64 v172, v[80:81]
	s_mov_b64 exec, -1
	s_cmp_lt_u32 s23, 2
	s_cbranch_scc1 .Lnp_Bf
	v_cmp_eq_u32_e64 s[6:7], 2, v168
	s_nop 0
	s_mov_b64 exec, s[6:7]
	ds_read_b64 v[82:83], v169
	ds_read_b64 v[84:85], v170
	ds_read_b64 v[86:87], v171
	s_mov_b64 exec, -1
	v_add_u32_sdwa v88, v116, v42 dst_sel:DWORD dst_unused:UNUSED_PAD src0_sel:DWORD src1_sel:WORD_0
	v_add_u32_sdwa v89, v116, v42 dst_sel:DWORD dst_unused:UNUSED_PAD src0_sel:DWORD src1_sel:WORD_1
	v_add_u32_sdwa v90, v116, v43 dst_sel:DWORD dst_unused:UNUSED_PAD src0_sel:DWORD src1_sel:WORD_0
	v_add_u32_sdwa v91, v116, v43 dst_sel:DWORD dst_unused:UNUSED_PAD src0_sel:DWORD src1_sel:WORD_1
	v_bfe_u32 v117, v41, 16, 7
	v_add_u32_sdwa v118, v116, v39 dst_sel:DWORD dst_unused:UNUSED_PAD src0_sel:DWORD src1_sel:WORD_0
	v_add_u32_sdwa v119, v116, v39 dst_sel:DWORD dst_unused:UNUSED_PAD src0_sel:DWORD src1_sel:WORD_1
	v_add_u32_sdwa v136, v116, v41 dst_sel:DWORD dst_unused:UNUSED_PAD src0_sel:DWORD src1_sel:WORD_0
	v_add_u32_e32 v156, 0xfffffa00, v156
	v_add_u32_e32 v137, 0xfffffe00, v172
	v_readlane_b32 s21, v60, s5
	v_max_i32_e32 v156, v156, v162
	v_lshl_add_u64 v[158:159], v[158:159], 0, s[2:3]
	s_or_b32 s10, s4, s21
	s_and_b32 s10, s10, 0x700
	s_and_b32 s9, s4, 0xff
	s_cselect_b32 s24, 0, 0x700
	s_or_b32 s10, s10, s24
	s_mov_b64 exec, s[6:7]
	s_waitcnt lgkmcnt(2)
	v_pk_fma_f32 v[80:81], v[48:49], v[82:83], v[78:79] op_sel_hi:[0,1,1]
	s_waitcnt lgkmcnt(1)
	v_pk_fma_f32 v[80:81], v[48:49], v[84:85], v[80:81] op_sel_hi:[0,1,1]
	s_waitcnt lgkmcnt(0)
	v_pk_fma_f32 v[80:81], v[48:49], v[86:87], v[80:81] op_sel_hi:[0,1,1]
	ds_write_b64 v172, v[80:81]
	s_mov_b64 exec, -1
	s_cmp_lt_u32 s23, 3
	s_cbranch_scc1 .Lbot_B
	s_mov_b32 s8, 3
